# v38 + expert-down GEMM: first-touch MFMAs take C=0 instead of a 127-instruction accumulator zero-fill per unit
# speedup vs baseline: 1.0079x; 1.0040x over previous
; template <class Epi, class Sched>
; __device__ __forceinline__ void gemm_phase(const int tid, LAS unsigned char* lds, const char* Abase, const int lda, const int ldb, const int K, const Sched& S, const Epi& E) {
;     ...
; #pragma unroll
;         for (int a = 0; a < 2; ++a)
; #pragma unroll
;             for (int b = 0; b < 2; ++b)
; #pragma unroll
;                 for (int m = 0; m < 4; ++m)
; #pragma unroll
;                     for (int n = 0; n < 2; ++n) acc[a][b][m][n] = (f32x4){0.f, 0.f, 0.f, 0.f};
;         cur = nxt; cB = nB; cA = nA; ++ui;
.LBB0_1705:
	s_andn2_b64 vcc, exec, s[46:47]
	s_cbranch_vccnz .LBB0_1716
	s_add_u32 s87, s56, 0x100
	v_mov_b32_e32 v209, v3
	v_mov_b32_e32 v207, v3
	s_addc_u32 s88, s57, 0
	s_mov_b32 s89, 0
	s_mov_b64 s[56:57], 0x10000
	s_branch .LBB0_1709

; #define PG8_STAGEA(bufoff, gbase, h) do { if constexpr (GATHER) { PG8_STAGE(bufoff, gbase, vA[h]); } else { PG8_STAGE(bufoff, (gbase) + (h) * hstepA, voffA); } } while (0)
; #define PG8_LDA(dst, b, h) do { _Pragma("unroll") for (int m = 0; m < 4; ++m) _Pragma("unroll") for (int k = 0; k < 2; ++k) dst[m][k] = *(const LAS bf16x8*)(lds + PG8_SA(b, h) + aoff + m * 2048 + k * 1024); } while (0)
; #define PG8_MM(ai, bj, At, Bt) do { if constexpr (Epi::F8MMA) PG8_MMA8(ai, bj, At, Bt##8); else PG8_MMA(ai, bj, At, Bt); } while (0)
; #define PG8_WAIT_V(n) asm volatile("s_waitcnt vmcnt(" #n ")" ::: "memory")
; #define PG8_WAIT_L(n) asm volatile("s_waitcnt lgkmcnt(" #n ")" ::: "memory")
; #define PG8_BAR __builtin_amdgcn_s_barrier()
; #define PG8_SCHED __builtin_amdgcn_sched_barrier(0)
; template <class Epi, class Sched>
; __device__ __forceinline__ void gemm_phase(const int tid, LAS unsigned char* lds, const char* Abase, const int lda, const int ldb, const int K, const Sched& S, const Epi& E) {
;     ...
;         for (int t = 0; t < nt; t += 2) {
;             const bool last = (t == nt - 2);
;             const char* a1 = cA + (size_t)(t + 1) * kstepA;
;             const char* a2 = last ? nA : cA + (size_t)(t + 2) * kstepA; const char* b2 = last ? nB : cB + (size_t)(t + 2) * kstep;
;             const char* a3 = a2 + kstepA; const char* b3 = b2 + kstep;
;             PG8_LDB(B0, 0, 0); PG8_LDB(B1, 0, 1); PG8_SCHED; PG8_LDA(At, 0, 0); PG8_STAGEA(PG8_SA(1, 1), a1, 1);
;             if constexpr (GATHER) { if (last) {
; #pragma unroll
;                 for (int h = 0; h < 2; ++h)
; #pragma unroll
;                     for (int i = 0; i < 2; ++i) vA[h][i] = vAn[h][i]; } }
;             PG8_WAIT_V(8); PG8_WAIT_L(0); PG8_BAR; PG8_MM(0, 0, At, B0); PG8_MM(0, 1, At, B1); PG8_BAR; PG8_SCHED;
;             PG8_LDA(At, 0, 1); PG8_STAGE(PG8_SB(0, 0), b2, voffB); PG8_STAGE(PG8_SB(0, 1), b2 + hstepB, voffB); PG8_STAGEA(PG8_SA(0, 0), a2, 0);
;             PG8_WAIT_V(8); PG8_WAIT_L(0); PG8_BAR; PG8_MM(1, 0, At, B0); PG8_MM(1, 1, At, B1); PG8_BAR; PG8_SCHED;
.LBB0_1708:
	s_add_i32 s89, s89, 2
	s_and_b64 s[60:61], s[62:63], exec
	s_cselect_b32 s61, 0, s56
	s_cselect_b32 s60, 0, s57
	s_add_u32 s66, s2, s61
	s_addc_u32 s67, s3, s60
	s_add_u32 s60, s66, 0x8000
	s_addc_u32 s61, s67, 0
	s_waitcnt vmcnt(8)
	s_and_b64 s[62:63], s[62:63], exec
	s_waitcnt lgkmcnt(0)
	s_cselect_b32 s62, s54, s87
	s_cselect_b32 s63, s55, s88
	s_add_u32 s64, s62, 0x80
	s_addc_u32 s65, s63, 0
	s_barrier
	s_setprio 1
	s_waitcnt lgkmcnt(0)
	v_mfma_scale_f32_16x16x128_f8f6f4 v[192:195], v[20:27], v[60:67], 0, v224, v216 op_sel_hi:[0,0,0]
	v_mfma_scale_f32_16x16x128_f8f6f4 v[188:191], v[28:35], v[60:67], 0, v224, v216 op_sel_hi:[0,0,0]
	v_mfma_scale_f32_16x16x128_f8f6f4 v[176:179], v[20:27], v[52:59], 0, v224, v216 op_sel_hi:[0,0,0]
	v_mfma_scale_f32_16x16x128_f8f6f4 v[172:175], v[28:35], v[52:59], 0, v224, v216 op_sel_hi:[0,0,0]
	v_mfma_scale_f32_16x16x128_f8f6f4 v[160:163], v[20:27], v[44:51], 0, v224, v216 op_sel_hi:[0,0,0]
	v_mfma_scale_f32_16x16x128_f8f6f4 v[156:159], v[28:35], v[44:51], 0, v224, v216 op_sel_hi:[0,0,0]
	v_mfma_scale_f32_16x16x128_f8f6f4 v[144:147], v[20:27], v[36:43], 0, v224, v216 op_sel_hi:[0,0,0]
	v_mfma_scale_f32_16x16x128_f8f6f4 v[140:143], v[28:35], v[36:43], 0, v224, v216 op_sel_hi:[0,0,0]
	s_setprio 0
	s_setprio 1
	v_mfma_scale_f32_16x16x128_f8f6f4 v[184:187], v[4:11], v[60:67], 0, v224, v216 op_sel_hi:[0,0,0]
	v_mfma_scale_f32_16x16x128_f8f6f4 v[180:183], v[12:19], v[60:67], 0, v224, v216 op_sel_hi:[0,0,0]
	v_mfma_scale_f32_16x16x128_f8f6f4 v[168:171], v[4:11], v[52:59], 0, v224, v216 op_sel_hi:[0,0,0]
	v_mfma_scale_f32_16x16x128_f8f6f4 v[164:167], v[12:19], v[52:59], 0, v224, v216 op_sel_hi:[0,0,0]
	v_mfma_scale_f32_16x16x128_f8f6f4 v[152:155], v[4:11], v[44:51], 0, v224, v216 op_sel_hi:[0,0,0]
	v_mfma_scale_f32_16x16x128_f8f6f4 v[148:151], v[12:19], v[44:51], 0, v224, v216 op_sel_hi:[0,0,0]
	v_mfma_scale_f32_16x16x128_f8f6f4 v[136:139], v[4:11], v[36:43], 0, v224, v216 op_sel_hi:[0,0,0]
	v_mfma_scale_f32_16x16x128_f8f6f4 v[132:135], v[12:19], v[36:43], 0, v224, v216 op_sel_hi:[0,0,0]
	s_setprio 0
	s_barrier
	s_mov_b32 m0, s28
	v_lshl_add_u64 v[228:229], s[62:63], 0, v[0:1]
	s_add_u32 s90, s62, 0x2000
	ds_read_b128 v[36:39], v243 offset:16384
	ds_read_b128 v[40:43], v243 offset:17408
	ds_read_b128 v[44:47], v243 offset:18432
	ds_read_b128 v[48:51], v243 offset:19456
	ds_read_b128 v[52:55], v243 offset:20480
	ds_read_b128 v[56:59], v243 offset:21504
	ds_read_b128 v[60:63], v243 offset:22528
	ds_read_b128 v[64:67], v243 offset:23552
	global_load_lds_dwordx4 v[228:229], off
	v_lshl_add_u64 v[228:229], s[62:63], 0, v[196:197]
	s_mov_b32 m0, s29
	s_addc_u32 s91, s63, 0
	global_load_lds_dwordx4 v[228:229], off
	v_lshl_add_u64 v[228:229], s[90:91], 0, v[0:1]
	s_mov_b32 m0, s68
	s_nop 0
	global_load_lds_dwordx4 v[228:229], off
	v_lshl_add_u64 v[228:229], s[90:91], 0, v[196:197]
	s_mov_b32 m0, s69
	s_nop 0
	global_load_lds_dwordx4 v[228:229], off
	s_mov_b32 m0, s25
	s_nop 0
	global_load_lds_dwordx4 v200, s[66:67]
	s_mov_b32 m0, s70
	s_nop 0
	global_load_lds_dwordx4 v198, s[66:67]
	s_waitcnt vmcnt(8)
	s_waitcnt lgkmcnt(0)
	s_barrier
	s_setprio 1
	s_waitcnt lgkmcnt(0)
	v_mfma_scale_f32_16x16x128_f8f6f4 v[128:131], v[20:27], v[36:43], 0, v224, v216 op_sel_hi:[0,0,0]
	v_mfma_scale_f32_16x16x128_f8f6f4 v[124:127], v[28:35], v[36:43], 0, v224, v216 op_sel_hi:[0,0,0]
	v_mfma_scale_f32_16x16x128_f8f6f4 v[112:115], v[20:27], v[44:51], 0, v224, v216 op_sel_hi:[0,0,0]
	v_mfma_scale_f32_16x16x128_f8f6f4 v[108:111], v[28:35], v[44:51], 0, v224, v216 op_sel_hi:[0,0,0]
	v_mfma_scale_f32_16x16x128_f8f6f4 v[96:99], v[20:27], v[52:59], 0, v224, v216 op_sel_hi:[0,0,0]
	v_mfma_scale_f32_16x16x128_f8f6f4 v[92:95], v[28:35], v[52:59], 0, v224, v216 op_sel_hi:[0,0,0]
	v_mfma_scale_f32_16x16x128_f8f6f4 v[80:83], v[20:27], v[60:67], 0, v224, v216 op_sel_hi:[0,0,0]
	v_mfma_scale_f32_16x16x128_f8f6f4 v[76:79], v[28:35], v[60:67], 0, v224, v216 op_sel_hi:[0,0,0]
	s_setprio 0
	s_setprio 1
	v_mfma_scale_f32_16x16x128_f8f6f4 v[120:123], v[4:11], v[36:43], 0, v224, v216 op_sel_hi:[0,0,0]
	v_mfma_scale_f32_16x16x128_f8f6f4 v[116:119], v[12:19], v[36:43], 0, v224, v216 op_sel_hi:[0,0,0]
	v_mfma_scale_f32_16x16x128_f8f6f4 v[104:107], v[4:11], v[44:51], 0, v224, v216 op_sel_hi:[0,0,0]
	v_mfma_scale_f32_16x16x128_f8f6f4 v[100:103], v[12:19], v[44:51], 0, v224, v216 op_sel_hi:[0,0,0]
	v_mfma_scale_f32_16x16x128_f8f6f4 v[88:91], v[4:11], v[52:59], 0, v224, v216 op_sel_hi:[0,0,0]
	v_mfma_scale_f32_16x16x128_f8f6f4 v[84:87], v[12:19], v[52:59], 0, v224, v216 op_sel_hi:[0,0,0]
	v_mfma_scale_f32_16x16x128_f8f6f4 v[72:75], v[4:11], v[60:67], 0, v224, v216 op_sel_hi:[0,0,0]
	v_mfma_scale_f32_16x16x128_f8f6f4 v[68:71], v[12:19], v[60:67], 0, v224, v216 op_sel_hi:[0,0,0]
	s_setprio 0
	s_barrier
	s_add_i32 s90, 0, 0x18000
	s_add_i32 s91, 0, 0x1c000
	v_add_u32_e32 v16, s90, v199
	v_add_u32_e32 v32, s91, v199
	ds_read_b128 v[4:7], v16
	ds_read_b128 v[8:11], v16 offset:1024
	ds_read_b128 v[12:15], v16 offset:2048
	ds_read_b128 v[16:19], v16 offset:3072
	ds_read_b128 v[20:23], v32
	ds_read_b128 v[24:27], v32 offset:1024
	ds_read_b128 v[28:31], v32 offset:2048
	ds_read_b128 v[32:35], v32 offset:3072
	s_mov_b32 m0, s71
	v_lshl_add_u64 v[212:213], s[66:67], 0, v[212:213]
	ds_read_b128 v[36:39], v243 offset:32768
	ds_read_b128 v[40:43], v243 offset:33792
	ds_read_b128 v[44:47], v243 offset:34816
	ds_read_b128 v[48:51], v243 offset:35840
	ds_read_b128 v[52:55], v243 offset:36864
	ds_read_b128 v[56:59], v243 offset:37888
	ds_read_b128 v[60:63], v243 offset:38912
	ds_read_b128 v[64:67], v243 offset:39936
	global_load_lds_dwordx4 v[212:213], off
	v_lshl_add_u64 v[210:211], s[66:67], 0, v[210:211]
	s_mov_b32 m0, s72
	s_nop 0
	global_load_lds_dwordx4 v[210:211], off
	s_waitcnt vmcnt(8)
	s_waitcnt lgkmcnt(0)
	s_barrier
; #define PG8_STAGEA(bufoff, gbase, h) do { if constexpr (GATHER) { PG8_STAGE(bufoff, gbase, vA[h]); } else { PG8_STAGE(bufoff, (gbase) + (h) * hstepA, voffA); } } while (0)
; #define PG8_LDA(dst, b, h) do { _Pragma("unroll") for (int m = 0; m < 4; ++m) _Pragma("unroll") for (int k = 0; k < 2; ++k) dst[m][k] = *(const LAS bf16x8*)(lds + PG8_SA(b, h) + aoff + m * 2048 + k * 1024); } while (0)
; #define PG8_MM(ai, bj, At, Bt) do { if constexpr (Epi::F8MMA) PG8_MMA8(ai, bj, At, Bt##8); else PG8_MMA(ai, bj, At, Bt); } while (0)
; #define PG8_WAIT_V(n) asm volatile("s_waitcnt vmcnt(" #n ")" ::: "memory")
; #define PG8_WAIT_L(n) asm volatile("s_waitcnt lgkmcnt(" #n ")" ::: "memory")
; #define PG8_BAR __builtin_amdgcn_s_barrier()
; #define PG8_SCHED __builtin_amdgcn_sched_barrier(0)
; template <class Epi, class Sched>
; __device__ __forceinline__ void gemm_phase(const int tid, LAS unsigned char* lds, const char* Abase, const int lda, const int ldb, const int K, const Sched& S, const Epi& E) {
;     ...
;             PG8_LDB(B0, 1, 0); PG8_LDB(B1, 1, 1); PG8_SCHED; PG8_LDA(At, 1, 0); PG8_STAGEA(PG8_SA(0, 1), a2, 1);
;             PG8_WAIT_V(8); PG8_WAIT_L(0); PG8_BAR; PG8_MM(0, 0, At, B0); PG8_MM(0, 1, At, B1); PG8_BAR; PG8_SCHED;
;             PG8_LDA(At, 1, 1); PG8_STAGE(PG8_SB(1, 0), b3, voffB); PG8_STAGE(PG8_SB(1, 1), b3 + hstepB, voffB); PG8_STAGEA(PG8_SA(1, 0), a3, 0);
;             PG8_WAIT_V(8); PG8_WAIT_L(0); PG8_BAR; PG8_MM(1, 0, At, B0); PG8_MM(1, 1, At, B1); PG8_BAR; PG8_SCHED;
	s_setprio 1
	s_waitcnt lgkmcnt(0)
	v_mfma_scale_f32_16x16x128_f8f6f4 v[192:195], v[4:11], v[36:43], v[192:195], v224, v216 op_sel_hi:[0,0,0]
	v_mfma_scale_f32_16x16x128_f8f6f4 v[188:191], v[12:19], v[36:43], v[188:191], v224, v216 op_sel_hi:[0,0,0]
	v_mfma_scale_f32_16x16x128_f8f6f4 v[176:179], v[4:11], v[44:51], v[176:179], v224, v216 op_sel_hi:[0,0,0]
	v_mfma_scale_f32_16x16x128_f8f6f4 v[172:175], v[12:19], v[44:51], v[172:175], v224, v216 op_sel_hi:[0,0,0]
	v_mfma_scale_f32_16x16x128_f8f6f4 v[160:163], v[4:11], v[52:59], v[160:163], v224, v216 op_sel_hi:[0,0,0]
	v_mfma_scale_f32_16x16x128_f8f6f4 v[156:159], v[12:19], v[52:59], v[156:159], v224, v216 op_sel_hi:[0,0,0]
	v_mfma_scale_f32_16x16x128_f8f6f4 v[144:147], v[4:11], v[60:67], v[144:147], v224, v216 op_sel_hi:[0,0,0]
	v_mfma_scale_f32_16x16x128_f8f6f4 v[140:143], v[12:19], v[60:67], v[140:143], v224, v216 op_sel_hi:[0,0,0]
	s_setprio 0
	s_setprio 1
	v_mfma_scale_f32_16x16x128_f8f6f4 v[184:187], v[20:27], v[36:43], v[184:187], v224, v216 op_sel_hi:[0,0,0]
	v_mfma_scale_f32_16x16x128_f8f6f4 v[180:183], v[28:35], v[36:43], v[180:183], v224, v216 op_sel_hi:[0,0,0]
	v_mfma_scale_f32_16x16x128_f8f6f4 v[168:171], v[20:27], v[44:51], v[168:171], v224, v216 op_sel_hi:[0,0,0]
	v_mfma_scale_f32_16x16x128_f8f6f4 v[164:167], v[28:35], v[44:51], v[164:167], v224, v216 op_sel_hi:[0,0,0]
	v_mfma_scale_f32_16x16x128_f8f6f4 v[152:155], v[20:27], v[52:59], v[152:155], v224, v216 op_sel_hi:[0,0,0]
	v_mfma_scale_f32_16x16x128_f8f6f4 v[148:151], v[28:35], v[52:59], v[148:151], v224, v216 op_sel_hi:[0,0,0]
	v_mfma_scale_f32_16x16x128_f8f6f4 v[136:139], v[20:27], v[60:67], v[136:139], v224, v216 op_sel_hi:[0,0,0]
	v_mfma_scale_f32_16x16x128_f8f6f4 v[132:135], v[28:35], v[60:67], v[132:135], v224, v216 op_sel_hi:[0,0,0]
	s_setprio 0
	s_barrier
	s_add_i32 s66, s90, s22
	v_lshl_add_u64 v[210:211], s[64:65], 0, v[0:1]
	s_mov_b32 m0, s66
	ds_read_b128 v[36:39], v243 offset:49152
	ds_read_b128 v[40:43], v243 offset:50176
	ds_read_b128 v[44:47], v243 offset:51200
	ds_read_b128 v[48:51], v243 offset:52224
	ds_read_b128 v[52:55], v243 offset:53248
	ds_read_b128 v[56:59], v243 offset:54272
	ds_read_b128 v[60:63], v243 offset:55296
	ds_read_b128 v[64:67], v243 offset:56320
	global_load_lds_dwordx4 v[210:211], off
	s_add_i32 m0, s66, 0x2000
	s_add_u32 s62, s62, 0x2080
	v_lshl_add_u64 v[210:211], s[64:65], 0, v[196:197]
	s_addc_u32 s63, s63, 0
	s_add_i32 s64, s91, s22
	global_load_lds_dwordx4 v[210:211], off
	v_lshl_add_u64 v[210:211], s[62:63], 0, v[0:1]
	s_mov_b32 m0, s64
	s_nop 0
	global_load_lds_dwordx4 v[210:211], off
	v_lshl_add_u64 v[210:211], s[62:63], 0, v[196:197]
	s_add_i32 m0, s64, 0x2000
	s_nop 0
	global_load_lds_dwordx4 v[210:211], off
	s_mov_b32 m0, s73
	s_nop 0
	global_load_lds_dwordx4 v200, s[60:61]
	s_mov_b32 m0, s76
	s_nop 0
	global_load_lds_dwordx4 v198, s[60:61]
	s_waitcnt vmcnt(8)
	s_waitcnt lgkmcnt(0)
	s_barrier
	s_setprio 1
	s_waitcnt lgkmcnt(0)
	v_mfma_scale_f32_16x16x128_f8f6f4 v[128:131], v[4:11], v[36:43], v[128:131], v224, v216 op_sel_hi:[0,0,0]
	v_mfma_scale_f32_16x16x128_f8f6f4 v[124:127], v[12:19], v[36:43], v[124:127], v224, v216 op_sel_hi:[0,0,0]
	v_mfma_scale_f32_16x16x128_f8f6f4 v[112:115], v[4:11], v[44:51], v[112:115], v224, v216 op_sel_hi:[0,0,0]
	v_mfma_scale_f32_16x16x128_f8f6f4 v[108:111], v[12:19], v[44:51], v[108:111], v224, v216 op_sel_hi:[0,0,0]
	v_mfma_scale_f32_16x16x128_f8f6f4 v[96:99], v[4:11], v[52:59], v[96:99], v224, v216 op_sel_hi:[0,0,0]
	v_mfma_scale_f32_16x16x128_f8f6f4 v[92:95], v[12:19], v[52:59], v[92:95], v224, v216 op_sel_hi:[0,0,0]
	v_mfma_scale_f32_16x16x128_f8f6f4 v[80:83], v[4:11], v[60:67], v[80:83], v224, v216 op_sel_hi:[0,0,0]
	v_mfma_scale_f32_16x16x128_f8f6f4 v[76:79], v[12:19], v[60:67], v[76:79], v224, v216 op_sel_hi:[0,0,0]
	s_setprio 0
	s_setprio 1
	v_mfma_scale_f32_16x16x128_f8f6f4 v[120:123], v[20:27], v[36:43], v[120:123], v224, v216 op_sel_hi:[0,0,0]
	v_mfma_scale_f32_16x16x128_f8f6f4 v[116:119], v[28:35], v[36:43], v[116:119], v224, v216 op_sel_hi:[0,0,0]
	v_mfma_scale_f32_16x16x128_f8f6f4 v[104:107], v[20:27], v[44:51], v[104:107], v224, v216 op_sel_hi:[0,0,0]
	v_mfma_scale_f32_16x16x128_f8f6f4 v[100:103], v[28:35], v[44:51], v[100:103], v224, v216 op_sel_hi:[0,0,0]
	v_mfma_scale_f32_16x16x128_f8f6f4 v[88:91], v[20:27], v[52:59], v[88:91], v224, v216 op_sel_hi:[0,0,0]
	v_mfma_scale_f32_16x16x128_f8f6f4 v[84:87], v[28:35], v[52:59], v[84:87], v224, v216 op_sel_hi:[0,0,0]
	v_mfma_scale_f32_16x16x128_f8f6f4 v[72:75], v[20:27], v[60:67], v[72:75], v224, v216 op_sel_hi:[0,0,0]
	v_mfma_scale_f32_16x16x128_f8f6f4 v[68:71], v[28:35], v[60:67], v[68:71], v224, v216 op_sel_hi:[0,0,0]
	s_setprio 0
	s_barrier
	s_add_u32 s87, s87, 0x100
	s_addc_u32 s88, s88, 0
	s_add_u32 s56, s56, 0x10000
	s_addc_u32 s57, s57, 0
	s_cmp_ge_i32 s89, s5
	s_cbranch_scc1 .LBB0_1711
